# baseline (speedup 1.0000x reference)
_Z15score_ds_kernelPKfS0_S0_S0_S0_S0_PfPKDF16_:
	v_readfirstlane_b32 s32, v0
	s_cmp_lt_u32 s32, 0x100
	s_cbranch_scc1 .Lsds_noprio
	s_setprio 1
.Lsds_noprio:
	s_load_dwordx2 s[26:27], s[0:1], 0x38
	s_bfe_u32 s28, s2, 0x10003
	s_mul_i32 s28, s28, 0x1a400
	v_lshlrev_b32_e32 v254, 4, v0
	v_mov_b32_e32 v255, 0
	v_readfirstlane_b32 s29, v0
	s_mov_b64 s[30:31], 0x2000
	s_waitcnt lgkmcnt(0)
	s_add_u32 s26, s26, s28
	s_addc_u32 s27, s27, 0
	s_lshl_b32 s28, s29, 4
	v_lshl_add_u64 v[254:255], s[26:27], 0, v[254:255]
	s_mov_b32 m0, s28
	s_add_u32 s28, s28, 0x2000
	global_load_lds_dwordx4 v[254:255], off
	v_lshl_add_u64 v[254:255], v[254:255], 0, s[30:31]
	s_mov_b32 m0, s28
	s_add_u32 s28, s28, 0x2000
	global_load_lds_dwordx4 v[254:255], off
	v_lshl_add_u64 v[254:255], v[254:255], 0, s[30:31]
	s_mov_b32 m0, s28
	s_add_u32 s28, s28, 0x2000
	global_load_lds_dwordx4 v[254:255], off
	v_lshl_add_u64 v[254:255], v[254:255], 0, s[30:31]
	s_mov_b32 m0, s28
	s_add_u32 s28, s28, 0x2000
	global_load_lds_dwordx4 v[254:255], off
	v_lshl_add_u64 v[254:255], v[254:255], 0, s[30:31]
	s_mov_b32 m0, s28
	s_add_u32 s28, s28, 0x2000
	global_load_lds_dwordx4 v[254:255], off
	v_lshl_add_u64 v[254:255], v[254:255], 0, s[30:31]
	s_mov_b32 m0, s28
	s_add_u32 s28, s28, 0x2000
	global_load_lds_dwordx4 v[254:255], off
	v_lshl_add_u64 v[254:255], v[254:255], 0, s[30:31]
	s_mov_b32 m0, s28
	s_add_u32 s28, s28, 0x2000
	global_load_lds_dwordx4 v[254:255], off
	v_lshl_add_u64 v[254:255], v[254:255], 0, s[30:31]
	s_mov_b32 m0, s28
	s_add_u32 s28, s28, 0x2000
	global_load_lds_dwordx4 v[254:255], off
	v_lshl_add_u64 v[254:255], v[254:255], 0, s[30:31]
	s_mov_b32 m0, s28
	s_add_u32 s28, s28, 0x2000
	global_load_lds_dwordx4 v[254:255], off
	v_lshl_add_u64 v[254:255], v[254:255], 0, s[30:31]
	s_mov_b32 m0, s28
	s_add_u32 s28, s28, 0x2000
	global_load_lds_dwordx4 v[254:255], off
	v_lshl_add_u64 v[254:255], v[254:255], 0, s[30:31]
	s_mov_b32 m0, s28
	s_add_u32 s28, s28, 0x2000
	global_load_lds_dwordx4 v[254:255], off
	v_lshl_add_u64 v[254:255], v[254:255], 0, s[30:31]
	s_mov_b32 m0, s28
	s_add_u32 s28, s28, 0x2000
	global_load_lds_dwordx4 v[254:255], off
	v_lshl_add_u64 v[254:255], v[254:255], 0, s[30:31]
	s_mov_b32 m0, s28
	s_add_u32 s28, s28, 0x2000
	global_load_lds_dwordx4 v[254:255], off
	v_lshl_add_u64 v[254:255], v[254:255], 0, s[30:31]
	s_cmp_lg_u32 s29, 0
	s_cbranch_scc1 .Lsds_dma_done
	s_mov_b32 m0, s28
	s_nop 0
	global_load_lds_dwordx4 v[254:255], off
